# v50 + selected branch: the first S tile's 16 v_exp moved from the end of the QK/softmax half-step to the head of the P.V half-step (half-step balance)
# speedup vs baseline: 1.0045x; 1.0045x over previous
.LBB0_1736:
	v_mul_f32_e32 v2, 0xbe0293ee, v175
	v_cndmask_b32_e64 v2, v168, v2, s[98:99]
	v_fma_f32 v68, v68, s2, v2
	v_fma_f32 v69, v69, s2, v2
	v_fma_f32 v70, v70, s2, v2
	v_fma_f32 v71, v71, s2, v2
	v_fma_f32 v72, v72, s2, v2
	v_fma_f32 v73, v73, s2, v2
	v_fma_f32 v74, v74, s2, v2
	v_fma_f32 v75, v75, s2, v2
	v_fma_f32 v76, v76, s2, v2
	v_fma_f32 v77, v77, s2, v2
	v_fma_f32 v78, v78, s2, v2
	v_fma_f32 v79, v79, s2, v2
	v_fma_f32 v80, v80, s2, v2
	v_fma_f32 v81, v81, s2, v2
	v_fma_f32 v82, v82, s2, v2
	v_fma_f32 v83, v83, s2, v2
	v_fma_f32 v86, v86, s2, v2
	v_fma_f32 v87, v87, s2, v2
	v_fma_f32 v84, v84, s2, v2
	v_fma_f32 v85, v85, s2, v2
	v_fma_f32 v88, v88, s2, v2
	v_fma_f32 v89, v89, s2, v2
	v_fma_f32 v90, v90, s2, v2
	v_fma_f32 v91, v91, s2, v2
	v_fma_f32 v92, v92, s2, v2
	v_fma_f32 v93, v93, s2, v2
	v_fma_f32 v94, v94, s2, v2
	v_fma_f32 v95, v95, s2, v2
	v_fma_f32 v96, v96, s2, v2
	v_fma_f32 v97, v97, s2, v2
	v_fma_f32 v98, v98, s2, v2
	v_fma_f32 v99, v99, s2, v2

.LBB0_1748:
	v_exp_f32_e32 v68, v68
	v_exp_f32_e32 v69, v69
	v_exp_f32_e32 v70, v70
	v_exp_f32_e32 v71, v71
	v_exp_f32_e32 v72, v72
	v_exp_f32_e32 v73, v73
	v_exp_f32_e32 v74, v74
	v_exp_f32_e32 v75, v75
	v_exp_f32_e32 v76, v76
	v_exp_f32_e32 v77, v77
	v_exp_f32_e32 v78, v78
	v_exp_f32_e32 v79, v79
	v_exp_f32_e32 v80, v80
	v_exp_f32_e32 v81, v81
	v_exp_f32_e32 v82, v82
	v_exp_f32_e32 v83, v83
	v_exp_f32_e32 v84, v84
	v_exp_f32_e32 v85, v85
	v_exp_f32_e32 v86, v86
	v_exp_f32_e32 v87, v87
	v_exp_f32_e32 v88, v88
	v_exp_f32_e32 v89, v89
	v_exp_f32_e32 v90, v90
	v_exp_f32_e32 v91, v91
	v_exp_f32_e32 v92, v92
	v_exp_f32_e32 v93, v93
	v_add_f32_e32 v194, v68, v84
	v_add_f32_e32 v195, v69, v85
	v_exp_f32_e32 v94, v94
	v_exp_f32_e32 v95, v95
	v_add_f32_e32 v192, v70, v86
	v_add_f32_e32 v193, v71, v87
	v_add_f32_e32 v194, 0, v194
	v_add_f32_e32 v195, 0, v195
	v_exp_f32_e32 v96, v96
	v_exp_f32_e32 v97, v97
	v_add_f32_e32 v190, v72, v88
	v_add_f32_e32 v191, v73, v89
	v_add_f32_e32 v192, v192, v194
	v_add_f32_e32 v193, v193, v195
	v_exp_f32_e32 v98, v98
	v_exp_f32_e32 v99, v99
	v_add_f32_e32 v188, v74, v90
	v_add_f32_e32 v189, v75, v91
	v_add_f32_e32 v190, v190, v192
	v_add_f32_e32 v191, v191, v193
	v_add_f32_e32 v186, v76, v92
	v_add_f32_e32 v187, v77, v93
	v_add_f32_e32 v188, v188, v190
	v_add_f32_e32 v189, v189, v191
	v_add_f32_e32 v184, v78, v94
	v_add_f32_e32 v185, v79, v95
	v_add_f32_e32 v186, v186, v188
	v_add_f32_e32 v187, v187, v189
	v_add_f32_e32 v182, v80, v96
	v_add_f32_e32 v183, v81, v97
	v_add_f32_e32 v184, v184, v186
	v_add_f32_e32 v185, v185, v187
	v_add_f32_e32 v180, v82, v98
	v_add_f32_e32 v181, v83, v99
	v_add_f32_e32 v182, v182, v184
	v_add_f32_e32 v183, v183, v185
	s_nop 0
	v_add_f32_e32 v180, v180, v182
	v_add_f32_e32 v181, v181, v183
	s_nop 0
	v_pk_add_f32 v[180:181], v[180:181], v[180:181] op_sel:[0,1] op_sel_hi:[1,0]
	s_nop 0
	v_mov_b32_e32 v1, v180
	s_nop 1
	v_permlane32_swap_b32_e32 v180, v1
	v_add_f32_e32 v1, v180, v1
	v_cvt_pk_bf16_f32 v180, v68, v69
	v_cvt_pk_bf16_f32 v181, v70, v71
	v_cvt_pk_bf16_f32 v182, v72, v73
	v_cvt_pk_bf16_f32 v183, v74, v75
	v_cvt_pk_bf16_f32 v184, v76, v77
	v_cvt_pk_bf16_f32 v185, v78, v79
	v_cvt_pk_bf16_f32 v186, v80, v81
	v_cvt_pk_bf16_f32 v187, v82, v83
	v_cvt_pk_bf16_f32 v188, v84, v85
	v_cvt_pk_bf16_f32 v189, v86, v87
	v_cvt_pk_bf16_f32 v190, v88, v89
	v_cvt_pk_bf16_f32 v191, v90, v91
	v_cvt_pk_bf16_f32 v192, v92, v93
	v_cvt_pk_bf16_f32 v193, v94, v95
	v_cvt_pk_bf16_f32 v194, v96, v97
	v_cvt_pk_bf16_f32 v195, v98, v99
	ds_read_b64_tr_b16 v[196:197], v0 offset:0
	ds_read_b64_tr_b16 v[198:199], v0 offset:0x800
	ds_read_b64_tr_b16 v[200:201], v0 offset:0x1000
	ds_read_b64_tr_b16 v[202:203], v0 offset:0x1800
	ds_read_b64_tr_b16 v[204:205], v0 offset:0x2000
	ds_read_b64_tr_b16 v[206:207], v0 offset:0x2800
	ds_read_b64_tr_b16 v[208:209], v0 offset:0x3000
	ds_read_b64_tr_b16 v[210:211], v0 offset:0x3800
	s_waitcnt lgkmcnt(0)
	v_fmac_f32_e32 v1, v138, v178
	v_permlane32_swap_b32_e32 v180, v182
	v_permlane32_swap_b32_e32 v181, v183
	v_permlane32_swap_b32_e32 v184, v186
	v_permlane32_swap_b32_e32 v185, v187
	v_permlane32_swap_b32_e32 v188, v190
	v_permlane32_swap_b32_e32 v189, v191
	v_permlane32_swap_b32_e32 v192, v194
	v_permlane32_swap_b32_e32 v193, v195
	v_mfma_f32_32x32x16_bf16 v[20:35], v[180:183], v[196:199], v[20:35]
	ds_read_b64_tr_b16 v[196:197], v0 offset:0x200
	ds_read_b64_tr_b16 v[198:199], v0 offset:0xa00
	v_mfma_f32_32x32x16_bf16 v[20:35], v[184:187], v[200:203], v[20:35]
	ds_read_b64_tr_b16 v[200:201], v0 offset:0x1200
	ds_read_b64_tr_b16 v[202:203], v0 offset:0x1a00
	v_mfma_f32_32x32x16_bf16 v[20:35], v[188:191], v[204:207], v[20:35]
	ds_read_b64_tr_b16 v[204:205], v0 offset:0x2200
	ds_read_b64_tr_b16 v[206:207], v0 offset:0x2a00
	v_mfma_f32_32x32x16_bf16 v[20:35], v[192:195], v[208:211], v[20:35]
	ds_read_b64_tr_b16 v[208:209], v0 offset:0x3200
	ds_read_b64_tr_b16 v[210:211], v0 offset:0x3a00
	s_waitcnt lgkmcnt(0)
	v_mfma_f32_32x32x16_bf16 v[36:51], v[180:183], v[196:199], v[36:51]
	ds_read_b64_tr_b16 v[196:197], v0 offset:0x400
	ds_read_b64_tr_b16 v[198:199], v0 offset:0xc00
	v_mfma_f32_32x32x16_bf16 v[36:51], v[184:187], v[200:203], v[36:51]
	ds_read_b64_tr_b16 v[200:201], v0 offset:0x1400
	ds_read_b64_tr_b16 v[202:203], v0 offset:0x1c00
	v_mfma_f32_32x32x16_bf16 v[36:51], v[188:191], v[204:207], v[36:51]
	ds_read_b64_tr_b16 v[204:205], v0 offset:0x2400
	ds_read_b64_tr_b16 v[206:207], v0 offset:0x2c00
	v_mfma_f32_32x32x16_bf16 v[36:51], v[192:195], v[208:211], v[36:51]
	ds_read_b64_tr_b16 v[208:209], v0 offset:0x3400
	ds_read_b64_tr_b16 v[210:211], v0 offset:0x3c00
	s_waitcnt lgkmcnt(0)
	v_mfma_f32_32x32x16_bf16 v[52:67], v[180:183], v[196:199], v[52:67]
	ds_read_b64_tr_b16 v[196:197], v0 offset:0x600
	ds_read_b64_tr_b16 v[198:199], v0 offset:0xe00
	v_mfma_f32_32x32x16_bf16 v[52:67], v[184:187], v[200:203], v[52:67]
	ds_read_b64_tr_b16 v[200:201], v0 offset:0x1600
	ds_read_b64_tr_b16 v[202:203], v0 offset:0x1e00
	v_mfma_f32_32x32x16_bf16 v[52:67], v[188:191], v[204:207], v[52:67]
	ds_read_b64_tr_b16 v[204:205], v0 offset:0x2600
	ds_read_b64_tr_b16 v[206:207], v0 offset:0x2e00
	v_mfma_f32_32x32x16_bf16 v[52:67], v[192:195], v[208:211], v[52:67]
	ds_read_b64_tr_b16 v[208:209], v0 offset:0x3600
	ds_read_b64_tr_b16 v[210:211], v0 offset:0x3e00
	s_waitcnt lgkmcnt(0)
	v_mfma_f32_32x32x16_bf16 v[4:19], v[180:183], v[196:199], v[4:19]
	v_mov_b32_e32 v138, v1
	v_mfma_f32_32x32x16_bf16 v[4:19], v[184:187], v[200:203], v[4:19]
	v_mfma_f32_32x32x16_bf16 v[4:19], v[188:191], v[204:207], v[4:19]
	v_mfma_f32_32x32x16_bf16 v[4:19], v[192:195], v[208:211], v[4:19]

.LBB0_1776:
	v_exp_f32_e32 v68, v68
	v_exp_f32_e32 v69, v69
	v_exp_f32_e32 v70, v70
	v_exp_f32_e32 v71, v71
	v_exp_f32_e32 v72, v72
	v_exp_f32_e32 v73, v73
	v_exp_f32_e32 v74, v74
	v_exp_f32_e32 v75, v75
	v_exp_f32_e32 v76, v76
	v_exp_f32_e32 v77, v77
	v_exp_f32_e32 v78, v78
	v_exp_f32_e32 v79, v79
	v_exp_f32_e32 v80, v80
	v_exp_f32_e32 v81, v81
	v_exp_f32_e32 v82, v82
	v_exp_f32_e32 v83, v83
	v_exp_f32_e32 v84, v84
	v_exp_f32_e32 v85, v85
	v_exp_f32_e32 v86, v86
	v_exp_f32_e32 v87, v87
	v_exp_f32_e32 v88, v88
	v_exp_f32_e32 v89, v89
	v_exp_f32_e32 v90, v90
	v_exp_f32_e32 v91, v91
	v_exp_f32_e32 v92, v92
	v_exp_f32_e32 v93, v93
	v_add_f32_e32 v194, v68, v84
	v_add_f32_e32 v195, v69, v85
	v_exp_f32_e32 v94, v94
	v_exp_f32_e32 v95, v95
	v_add_f32_e32 v192, v70, v86
	v_add_f32_e32 v193, v71, v87
	v_add_f32_e32 v194, 0, v194
	v_add_f32_e32 v195, 0, v195
	v_exp_f32_e32 v96, v96
	v_exp_f32_e32 v97, v97
	v_add_f32_e32 v190, v72, v88
	v_add_f32_e32 v191, v73, v89
	v_add_f32_e32 v192, v192, v194
	v_add_f32_e32 v193, v193, v195
	v_exp_f32_e32 v98, v98
	v_exp_f32_e32 v99, v99
	v_add_f32_e32 v188, v74, v90
	v_add_f32_e32 v189, v75, v91
	v_add_f32_e32 v190, v190, v192
	v_add_f32_e32 v191, v191, v193
	v_add_f32_e32 v186, v76, v92
	v_add_f32_e32 v187, v77, v93
	v_add_f32_e32 v188, v188, v190
	v_add_f32_e32 v189, v189, v191
	v_add_f32_e32 v184, v78, v94
	v_add_f32_e32 v185, v79, v95
	v_add_f32_e32 v186, v186, v188
	v_add_f32_e32 v187, v187, v189
	v_add_f32_e32 v182, v80, v96
	v_add_f32_e32 v183, v81, v97
	v_add_f32_e32 v184, v184, v186
	v_add_f32_e32 v185, v185, v187
	v_add_f32_e32 v180, v82, v98
	v_add_f32_e32 v181, v83, v99
	v_add_f32_e32 v182, v182, v184
	v_add_f32_e32 v183, v183, v185
	s_nop 0
	v_add_f32_e32 v180, v180, v182
	v_add_f32_e32 v181, v181, v183
	s_nop 0
	v_pk_add_f32 v[180:181], v[180:181], v[180:181] op_sel:[0,1] op_sel_hi:[1,0]
	s_nop 0
	v_mov_b32_e32 v1, v180
	s_nop 1
	v_permlane32_swap_b32_e32 v180, v1
	v_add_f32_e32 v1, v180, v1
	v_cvt_pk_bf16_f32 v180, v68, v69
	v_cvt_pk_bf16_f32 v181, v70, v71
	v_cvt_pk_bf16_f32 v182, v72, v73
	v_cvt_pk_bf16_f32 v183, v74, v75
	v_cvt_pk_bf16_f32 v184, v76, v77
	v_cvt_pk_bf16_f32 v185, v78, v79
	v_cvt_pk_bf16_f32 v186, v80, v81
	v_cvt_pk_bf16_f32 v187, v82, v83
	v_cvt_pk_bf16_f32 v188, v84, v85
	v_cvt_pk_bf16_f32 v189, v86, v87
	v_cvt_pk_bf16_f32 v190, v88, v89
	v_cvt_pk_bf16_f32 v191, v90, v91
	v_cvt_pk_bf16_f32 v192, v92, v93
	v_cvt_pk_bf16_f32 v193, v94, v95
	v_cvt_pk_bf16_f32 v194, v96, v97
	v_cvt_pk_bf16_f32 v195, v98, v99
	ds_read_b64_tr_b16 v[196:197], v136 offset:0
	ds_read_b64_tr_b16 v[198:199], v136 offset:0x800
	ds_read_b64_tr_b16 v[200:201], v136 offset:0x1000
	ds_read_b64_tr_b16 v[202:203], v136 offset:0x1800
	ds_read_b64_tr_b16 v[204:205], v136 offset:0x2000
	ds_read_b64_tr_b16 v[206:207], v136 offset:0x2800
	ds_read_b64_tr_b16 v[208:209], v136 offset:0x3000
	ds_read_b64_tr_b16 v[210:211], v136 offset:0x3800
	s_waitcnt lgkmcnt(0)
	v_fmac_f32_e32 v1, v138, v178
	v_permlane32_swap_b32_e32 v180, v182
	v_permlane32_swap_b32_e32 v181, v183
	v_permlane32_swap_b32_e32 v184, v186
	v_permlane32_swap_b32_e32 v185, v187
	v_permlane32_swap_b32_e32 v188, v190
	v_permlane32_swap_b32_e32 v189, v191
	v_permlane32_swap_b32_e32 v192, v194
	v_permlane32_swap_b32_e32 v193, v195
	v_mfma_f32_32x32x16_bf16 v[20:35], v[180:183], v[196:199], v[20:35]
	ds_read_b64_tr_b16 v[196:197], v136 offset:0x200
	ds_read_b64_tr_b16 v[198:199], v136 offset:0xa00
	v_mfma_f32_32x32x16_bf16 v[20:35], v[184:187], v[200:203], v[20:35]
	ds_read_b64_tr_b16 v[200:201], v136 offset:0x1200
	ds_read_b64_tr_b16 v[202:203], v136 offset:0x1a00
	v_mfma_f32_32x32x16_bf16 v[20:35], v[188:191], v[204:207], v[20:35]
	ds_read_b64_tr_b16 v[204:205], v136 offset:0x2200
	ds_read_b64_tr_b16 v[206:207], v136 offset:0x2a00
	v_mfma_f32_32x32x16_bf16 v[20:35], v[192:195], v[208:211], v[20:35]
	ds_read_b64_tr_b16 v[208:209], v136 offset:0x3200
	ds_read_b64_tr_b16 v[210:211], v136 offset:0x3a00
	s_waitcnt lgkmcnt(0)
	v_mfma_f32_32x32x16_bf16 v[36:51], v[180:183], v[196:199], v[36:51]
	ds_read_b64_tr_b16 v[196:197], v136 offset:0x400
	ds_read_b64_tr_b16 v[198:199], v136 offset:0xc00
	v_mfma_f32_32x32x16_bf16 v[36:51], v[184:187], v[200:203], v[36:51]
	ds_read_b64_tr_b16 v[200:201], v136 offset:0x1400
	ds_read_b64_tr_b16 v[202:203], v136 offset:0x1c00
	v_mfma_f32_32x32x16_bf16 v[36:51], v[188:191], v[204:207], v[36:51]
	ds_read_b64_tr_b16 v[204:205], v136 offset:0x2400
	ds_read_b64_tr_b16 v[206:207], v136 offset:0x2c00
	v_mfma_f32_32x32x16_bf16 v[36:51], v[192:195], v[208:211], v[36:51]
	ds_read_b64_tr_b16 v[208:209], v136 offset:0x3400
	ds_read_b64_tr_b16 v[210:211], v136 offset:0x3c00
	s_waitcnt lgkmcnt(0)
	v_mfma_f32_32x32x16_bf16 v[52:67], v[180:183], v[196:199], v[52:67]
	ds_read_b64_tr_b16 v[196:197], v136 offset:0x600
	ds_read_b64_tr_b16 v[198:199], v136 offset:0xe00
	v_mfma_f32_32x32x16_bf16 v[52:67], v[184:187], v[200:203], v[52:67]
	ds_read_b64_tr_b16 v[200:201], v136 offset:0x1600
	ds_read_b64_tr_b16 v[202:203], v136 offset:0x1e00
	v_mfma_f32_32x32x16_bf16 v[52:67], v[188:191], v[204:207], v[52:67]
	ds_read_b64_tr_b16 v[204:205], v136 offset:0x2600
	ds_read_b64_tr_b16 v[206:207], v136 offset:0x2e00
	v_mfma_f32_32x32x16_bf16 v[52:67], v[192:195], v[208:211], v[52:67]
	ds_read_b64_tr_b16 v[208:209], v136 offset:0x3600
	ds_read_b64_tr_b16 v[210:211], v136 offset:0x3e00
	s_waitcnt lgkmcnt(0)
	v_mfma_f32_32x32x16_bf16 v[4:19], v[180:183], v[196:199], v[4:19]
	v_mov_b32_e32 v138, v1
	v_mfma_f32_32x32x16_bf16 v[4:19], v[184:187], v[200:203], v[4:19]
	v_mfma_f32_32x32x16_bf16 v[4:19], v[188:191], v[204:207], v[4:19]
	v_mfma_f32_32x32x16_bf16 v[4:19], v[192:195], v[208:211], v[4:19]

.LBB0_1831:
	v_mul_f32_e32 v2, 0xbe0293ee, v154
	v_cndmask_b32_e64 v2, v168, v2, s[98:99]
	v_fma_f32 v68, v68, s2, v2
	v_fma_f32 v69, v69, s2, v2
	v_fma_f32 v70, v70, s2, v2
	v_fma_f32 v71, v71, s2, v2
	v_fma_f32 v72, v72, s2, v2
	v_fma_f32 v73, v73, s2, v2
	v_fma_f32 v74, v74, s2, v2
	v_fma_f32 v75, v75, s2, v2
	v_fma_f32 v76, v76, s2, v2
	v_fma_f32 v77, v77, s2, v2
	v_fma_f32 v78, v78, s2, v2
	v_fma_f32 v79, v79, s2, v2
	v_fma_f32 v80, v80, s2, v2
	v_fma_f32 v81, v81, s2, v2
	v_fma_f32 v82, v82, s2, v2
	v_fma_f32 v83, v83, s2, v2
	v_fma_f32 v86, v86, s2, v2
	v_fma_f32 v87, v87, s2, v2
	v_fma_f32 v84, v84, s2, v2
	v_fma_f32 v85, v85, s2, v2
	v_fma_f32 v88, v88, s2, v2
	v_fma_f32 v89, v89, s2, v2
	v_fma_f32 v90, v90, s2, v2
	v_fma_f32 v91, v91, s2, v2
	v_fma_f32 v92, v92, s2, v2
	v_fma_f32 v93, v93, s2, v2
	v_fma_f32 v94, v94, s2, v2
	v_fma_f32 v95, v95, s2, v2
	v_fma_f32 v96, v96, s2, v2
	v_fma_f32 v97, v97, s2, v2
	v_fma_f32 v98, v98, s2, v2
	v_fma_f32 v99, v99, s2, v2

.LBB0_1843:
	v_exp_f32_e32 v68, v68
	v_exp_f32_e32 v69, v69
	v_exp_f32_e32 v70, v70
	v_exp_f32_e32 v71, v71
	v_exp_f32_e32 v72, v72
	v_exp_f32_e32 v73, v73
	v_exp_f32_e32 v74, v74
	v_exp_f32_e32 v75, v75
	v_exp_f32_e32 v76, v76
	v_exp_f32_e32 v77, v77
	v_exp_f32_e32 v78, v78
	v_exp_f32_e32 v79, v79
	v_exp_f32_e32 v80, v80
	v_exp_f32_e32 v81, v81
	v_exp_f32_e32 v82, v82
	v_exp_f32_e32 v83, v83
	v_exp_f32_e32 v84, v84
	v_exp_f32_e32 v85, v85
	v_exp_f32_e32 v86, v86
	v_exp_f32_e32 v87, v87
	v_exp_f32_e32 v88, v88
	v_exp_f32_e32 v89, v89
	v_exp_f32_e32 v90, v90
	v_exp_f32_e32 v91, v91
	v_exp_f32_e32 v92, v92
	v_exp_f32_e32 v93, v93
	v_add_f32_e32 v184, v68, v84
	v_add_f32_e32 v185, v69, v85
	v_exp_f32_e32 v94, v94
	v_exp_f32_e32 v95, v95
	v_add_f32_e32 v182, v70, v86
	v_add_f32_e32 v183, v71, v87
	v_add_f32_e32 v184, 0, v184
	v_add_f32_e32 v185, 0, v185
	v_exp_f32_e32 v96, v96
	v_exp_f32_e32 v97, v97
	v_add_f32_e32 v180, v72, v88
	v_add_f32_e32 v181, v73, v89
	v_add_f32_e32 v182, v182, v184
	v_add_f32_e32 v183, v183, v185
	v_exp_f32_e32 v98, v98
	v_exp_f32_e32 v99, v99
	v_add_f32_e32 v178, v74, v90
	v_add_f32_e32 v179, v75, v91
	v_add_f32_e32 v180, v180, v182
	v_add_f32_e32 v181, v181, v183
	v_add_f32_e32 v176, v76, v92
	v_add_f32_e32 v177, v77, v93
	v_add_f32_e32 v178, v178, v180
	v_add_f32_e32 v179, v179, v181
	v_add_f32_e32 v174, v78, v94
	v_add_f32_e32 v175, v79, v95
	v_add_f32_e32 v176, v176, v178
	v_add_f32_e32 v177, v177, v179
	v_add_f32_e32 v172, v80, v96
	v_add_f32_e32 v173, v81, v97
	v_add_f32_e32 v174, v174, v176
	v_add_f32_e32 v175, v175, v177
	v_add_f32_e32 v170, v82, v98
	v_add_f32_e32 v171, v83, v99
	v_add_f32_e32 v172, v172, v174
	v_add_f32_e32 v173, v173, v175
	s_nop 0
	v_add_f32_e32 v170, v170, v172
	v_add_f32_e32 v171, v171, v173
	s_nop 0
	v_pk_add_f32 v[170:171], v[170:171], v[170:171] op_sel:[0,1] op_sel_hi:[1,0]
	s_nop 0
	v_mov_b32_e32 v1, v170
	s_nop 1
	v_permlane32_swap_b32_e32 v170, v1
	v_add_f32_e32 v1, v170, v1
	v_cvt_pk_bf16_f32 v170, v68, v69
	v_cvt_pk_bf16_f32 v171, v70, v71
	v_cvt_pk_bf16_f32 v172, v72, v73
	v_cvt_pk_bf16_f32 v173, v74, v75
	v_cvt_pk_bf16_f32 v174, v76, v77
	v_cvt_pk_bf16_f32 v175, v78, v79
	v_cvt_pk_bf16_f32 v176, v80, v81
	v_cvt_pk_bf16_f32 v177, v82, v83
	v_cvt_pk_bf16_f32 v178, v84, v85
	v_cvt_pk_bf16_f32 v179, v86, v87
	v_cvt_pk_bf16_f32 v180, v88, v89
	v_cvt_pk_bf16_f32 v181, v90, v91
	v_cvt_pk_bf16_f32 v182, v92, v93
	v_cvt_pk_bf16_f32 v183, v94, v95
	v_cvt_pk_bf16_f32 v184, v96, v97
	v_cvt_pk_bf16_f32 v185, v98, v99
	ds_read_b64_tr_b16 v[186:187], v0 offset:0
	ds_read_b64_tr_b16 v[188:189], v0 offset:0x800
	ds_read_b64_tr_b16 v[190:191], v0 offset:0x1000
	ds_read_b64_tr_b16 v[192:193], v0 offset:0x1800
	ds_read_b64_tr_b16 v[194:195], v0 offset:0x2000
	ds_read_b64_tr_b16 v[196:197], v0 offset:0x2800
	ds_read_b64_tr_b16 v[198:199], v0 offset:0x3000
	ds_read_b64_tr_b16 v[200:201], v0 offset:0x3800
	s_waitcnt lgkmcnt(0)
	v_fmac_f32_e32 v1, v138, v155
	v_permlane32_swap_b32_e32 v170, v172
	v_permlane32_swap_b32_e32 v171, v173
	v_permlane32_swap_b32_e32 v174, v176
	v_permlane32_swap_b32_e32 v175, v177
	v_permlane32_swap_b32_e32 v178, v180
	v_permlane32_swap_b32_e32 v179, v181
	v_permlane32_swap_b32_e32 v182, v184
	v_permlane32_swap_b32_e32 v183, v185
	v_mfma_f32_32x32x16_bf16 v[20:35], v[170:173], v[186:189], v[20:35]
	ds_read_b64_tr_b16 v[186:187], v0 offset:0x200
	ds_read_b64_tr_b16 v[188:189], v0 offset:0xa00
	v_mfma_f32_32x32x16_bf16 v[20:35], v[174:177], v[190:193], v[20:35]
	ds_read_b64_tr_b16 v[190:191], v0 offset:0x1200
	ds_read_b64_tr_b16 v[192:193], v0 offset:0x1a00
	v_mfma_f32_32x32x16_bf16 v[20:35], v[178:181], v[194:197], v[20:35]
	ds_read_b64_tr_b16 v[194:195], v0 offset:0x2200
	ds_read_b64_tr_b16 v[196:197], v0 offset:0x2a00
	v_mfma_f32_32x32x16_bf16 v[20:35], v[182:185], v[198:201], v[20:35]
	ds_read_b64_tr_b16 v[198:199], v0 offset:0x3200
	ds_read_b64_tr_b16 v[200:201], v0 offset:0x3a00
	s_waitcnt lgkmcnt(0)
	v_mfma_f32_32x32x16_bf16 v[36:51], v[170:173], v[186:189], v[36:51]
	ds_read_b64_tr_b16 v[186:187], v0 offset:0x400
	ds_read_b64_tr_b16 v[188:189], v0 offset:0xc00
	v_mfma_f32_32x32x16_bf16 v[36:51], v[174:177], v[190:193], v[36:51]
	ds_read_b64_tr_b16 v[190:191], v0 offset:0x1400
	ds_read_b64_tr_b16 v[192:193], v0 offset:0x1c00
	v_mfma_f32_32x32x16_bf16 v[36:51], v[178:181], v[194:197], v[36:51]
	ds_read_b64_tr_b16 v[194:195], v0 offset:0x2400
	ds_read_b64_tr_b16 v[196:197], v0 offset:0x2c00
	v_mfma_f32_32x32x16_bf16 v[36:51], v[182:185], v[198:201], v[36:51]
	ds_read_b64_tr_b16 v[198:199], v0 offset:0x3400
	ds_read_b64_tr_b16 v[200:201], v0 offset:0x3c00
	s_waitcnt lgkmcnt(0)
	v_mfma_f32_32x32x16_bf16 v[52:67], v[170:173], v[186:189], v[52:67]
	ds_read_b64_tr_b16 v[186:187], v0 offset:0x600
	ds_read_b64_tr_b16 v[188:189], v0 offset:0xe00
	v_mfma_f32_32x32x16_bf16 v[52:67], v[174:177], v[190:193], v[52:67]
	ds_read_b64_tr_b16 v[190:191], v0 offset:0x1600
	ds_read_b64_tr_b16 v[192:193], v0 offset:0x1e00
	v_mfma_f32_32x32x16_bf16 v[52:67], v[178:181], v[194:197], v[52:67]
	ds_read_b64_tr_b16 v[194:195], v0 offset:0x2600
	ds_read_b64_tr_b16 v[196:197], v0 offset:0x2e00
	v_mfma_f32_32x32x16_bf16 v[52:67], v[182:185], v[198:201], v[52:67]
	ds_read_b64_tr_b16 v[198:199], v0 offset:0x3600
	ds_read_b64_tr_b16 v[200:201], v0 offset:0x3e00
	s_waitcnt lgkmcnt(0)
	v_mfma_f32_32x32x16_bf16 v[4:19], v[170:173], v[186:189], v[4:19]
	v_mov_b32_e32 v138, v1
	v_mfma_f32_32x32x16_bf16 v[4:19], v[174:177], v[190:193], v[4:19]
	v_mfma_f32_32x32x16_bf16 v[4:19], v[178:181], v[194:197], v[4:19]
	v_mfma_f32_32x32x16_bf16 v[4:19], v[182:185], v[198:201], v[4:19]

.LBB0_1869:
	v_exp_f32_e32 v68, v68
	v_exp_f32_e32 v69, v69
	v_exp_f32_e32 v70, v70
	v_exp_f32_e32 v71, v71
	v_exp_f32_e32 v72, v72
	v_exp_f32_e32 v73, v73
	v_exp_f32_e32 v74, v74
	v_exp_f32_e32 v75, v75
	v_exp_f32_e32 v76, v76
	v_exp_f32_e32 v77, v77
	v_exp_f32_e32 v78, v78
	v_exp_f32_e32 v79, v79
	v_exp_f32_e32 v80, v80
	v_exp_f32_e32 v81, v81
	v_exp_f32_e32 v82, v82
	v_exp_f32_e32 v83, v83
	v_exp_f32_e32 v84, v84
	v_exp_f32_e32 v85, v85
	v_exp_f32_e32 v86, v86
	v_exp_f32_e32 v87, v87
	v_exp_f32_e32 v88, v88
	v_exp_f32_e32 v89, v89
	v_exp_f32_e32 v90, v90
	v_exp_f32_e32 v91, v91
	v_exp_f32_e32 v92, v92
	v_exp_f32_e32 v93, v93
	v_add_f32_e32 v184, v68, v84
	v_add_f32_e32 v185, v69, v85
	v_exp_f32_e32 v94, v94
	v_exp_f32_e32 v95, v95
	v_add_f32_e32 v182, v70, v86
	v_add_f32_e32 v183, v71, v87
	v_add_f32_e32 v184, 0, v184
	v_add_f32_e32 v185, 0, v185
	v_exp_f32_e32 v96, v96
	v_exp_f32_e32 v97, v97
	v_add_f32_e32 v180, v72, v88
	v_add_f32_e32 v181, v73, v89
	v_add_f32_e32 v182, v182, v184
	v_add_f32_e32 v183, v183, v185
	v_exp_f32_e32 v98, v98
	v_exp_f32_e32 v99, v99
	v_add_f32_e32 v178, v74, v90
	v_add_f32_e32 v179, v75, v91
	v_add_f32_e32 v180, v180, v182
	v_add_f32_e32 v181, v181, v183
	v_add_f32_e32 v176, v76, v92
	v_add_f32_e32 v177, v77, v93
	v_add_f32_e32 v178, v178, v180
	v_add_f32_e32 v179, v179, v181
	v_add_f32_e32 v174, v78, v94
	v_add_f32_e32 v175, v79, v95
	v_add_f32_e32 v176, v176, v178
	v_add_f32_e32 v177, v177, v179
	v_add_f32_e32 v172, v80, v96
	v_add_f32_e32 v173, v81, v97
	v_add_f32_e32 v174, v174, v176
	v_add_f32_e32 v175, v175, v177
	v_add_f32_e32 v170, v82, v98
	v_add_f32_e32 v171, v83, v99
	v_add_f32_e32 v172, v172, v174
	v_add_f32_e32 v173, v173, v175
	s_nop 0
	v_add_f32_e32 v170, v170, v172
	v_add_f32_e32 v171, v171, v173
	s_nop 0
	v_pk_add_f32 v[170:171], v[170:171], v[170:171] op_sel:[0,1] op_sel_hi:[1,0]
	s_nop 0
	v_mov_b32_e32 v1, v170
	s_nop 1
	v_permlane32_swap_b32_e32 v170, v1
	v_add_f32_e32 v1, v170, v1
	v_cvt_pk_bf16_f32 v170, v68, v69
	v_cvt_pk_bf16_f32 v171, v70, v71
	v_cvt_pk_bf16_f32 v172, v72, v73
	v_cvt_pk_bf16_f32 v173, v74, v75
	v_cvt_pk_bf16_f32 v174, v76, v77
	v_cvt_pk_bf16_f32 v175, v78, v79
	v_cvt_pk_bf16_f32 v176, v80, v81
	v_cvt_pk_bf16_f32 v177, v82, v83
	v_cvt_pk_bf16_f32 v178, v84, v85
	v_cvt_pk_bf16_f32 v179, v86, v87
	v_cvt_pk_bf16_f32 v180, v88, v89
	v_cvt_pk_bf16_f32 v181, v90, v91
	v_cvt_pk_bf16_f32 v182, v92, v93
	v_cvt_pk_bf16_f32 v183, v94, v95
	v_cvt_pk_bf16_f32 v184, v96, v97
	v_cvt_pk_bf16_f32 v185, v98, v99
	ds_read_b64_tr_b16 v[186:187], v136 offset:0
	ds_read_b64_tr_b16 v[188:189], v136 offset:0x800
	ds_read_b64_tr_b16 v[190:191], v136 offset:0x1000
	ds_read_b64_tr_b16 v[192:193], v136 offset:0x1800
	ds_read_b64_tr_b16 v[194:195], v136 offset:0x2000
	ds_read_b64_tr_b16 v[196:197], v136 offset:0x2800
	ds_read_b64_tr_b16 v[198:199], v136 offset:0x3000
	ds_read_b64_tr_b16 v[200:201], v136 offset:0x3800
	s_waitcnt lgkmcnt(0)
	v_fmac_f32_e32 v1, v138, v155
	v_permlane32_swap_b32_e32 v170, v172
	v_permlane32_swap_b32_e32 v171, v173
	v_permlane32_swap_b32_e32 v174, v176
	v_permlane32_swap_b32_e32 v175, v177
	v_permlane32_swap_b32_e32 v178, v180
	v_permlane32_swap_b32_e32 v179, v181
	v_permlane32_swap_b32_e32 v182, v184
	v_permlane32_swap_b32_e32 v183, v185
	v_mfma_f32_32x32x16_bf16 v[20:35], v[170:173], v[186:189], v[20:35]
	ds_read_b64_tr_b16 v[186:187], v136 offset:0x200
	ds_read_b64_tr_b16 v[188:189], v136 offset:0xa00
	v_mfma_f32_32x32x16_bf16 v[20:35], v[174:177], v[190:193], v[20:35]
	ds_read_b64_tr_b16 v[190:191], v136 offset:0x1200
	ds_read_b64_tr_b16 v[192:193], v136 offset:0x1a00
	v_mfma_f32_32x32x16_bf16 v[20:35], v[178:181], v[194:197], v[20:35]
	ds_read_b64_tr_b16 v[194:195], v136 offset:0x2200
	ds_read_b64_tr_b16 v[196:197], v136 offset:0x2a00
	v_mfma_f32_32x32x16_bf16 v[20:35], v[182:185], v[198:201], v[20:35]
	ds_read_b64_tr_b16 v[198:199], v136 offset:0x3200
	ds_read_b64_tr_b16 v[200:201], v136 offset:0x3a00
	s_waitcnt lgkmcnt(0)
	v_mfma_f32_32x32x16_bf16 v[36:51], v[170:173], v[186:189], v[36:51]
	ds_read_b64_tr_b16 v[186:187], v136 offset:0x400
	ds_read_b64_tr_b16 v[188:189], v136 offset:0xc00
	v_mfma_f32_32x32x16_bf16 v[36:51], v[174:177], v[190:193], v[36:51]
	ds_read_b64_tr_b16 v[190:191], v136 offset:0x1400
	ds_read_b64_tr_b16 v[192:193], v136 offset:0x1c00
	v_mfma_f32_32x32x16_bf16 v[36:51], v[178:181], v[194:197], v[36:51]
	ds_read_b64_tr_b16 v[194:195], v136 offset:0x2400
	ds_read_b64_tr_b16 v[196:197], v136 offset:0x2c00
	v_mfma_f32_32x32x16_bf16 v[36:51], v[182:185], v[198:201], v[36:51]
	ds_read_b64_tr_b16 v[198:199], v136 offset:0x3400
	ds_read_b64_tr_b16 v[200:201], v136 offset:0x3c00
	s_waitcnt lgkmcnt(0)
	v_mfma_f32_32x32x16_bf16 v[52:67], v[170:173], v[186:189], v[52:67]
	ds_read_b64_tr_b16 v[186:187], v136 offset:0x600
	ds_read_b64_tr_b16 v[188:189], v136 offset:0xe00
	v_mfma_f32_32x32x16_bf16 v[52:67], v[174:177], v[190:193], v[52:67]
	ds_read_b64_tr_b16 v[190:191], v136 offset:0x1600
	ds_read_b64_tr_b16 v[192:193], v136 offset:0x1e00
	v_mfma_f32_32x32x16_bf16 v[52:67], v[178:181], v[194:197], v[52:67]
	ds_read_b64_tr_b16 v[194:195], v136 offset:0x2600
	ds_read_b64_tr_b16 v[196:197], v136 offset:0x2e00
	v_mfma_f32_32x32x16_bf16 v[52:67], v[182:185], v[198:201], v[52:67]
	ds_read_b64_tr_b16 v[198:199], v136 offset:0x3600
	ds_read_b64_tr_b16 v[200:201], v136 offset:0x3e00
	s_waitcnt lgkmcnt(0)
	v_mfma_f32_32x32x16_bf16 v[4:19], v[170:173], v[186:189], v[4:19]
	v_mov_b32_e32 v138, v1
	v_mfma_f32_32x32x16_bf16 v[4:19], v[174:177], v[190:193], v[4:19]
	v_mfma_f32_32x32x16_bf16 v[4:19], v[178:181], v[194:197], v[4:19]
	v_mfma_f32_32x32x16_bf16 v[4:19], v[182:185], v[198:201], v[4:19]
